# MoE phases: store-ack drain and duplicate rendezvous between the DOWN and UP GEMMs of one phase removed (on top of early-invalidate + release broadcast barrier)
# speedup vs baseline: 1.0005x; 1.0005x over previous
; #define PG8_WAIT_V(n) asm volatile("s_waitcnt vmcnt(" #n ")" ::: "memory")
; #define PG8_BAR __builtin_amdgcn_s_barrier()
;     ...
;     PG8_WAIT_V(0);
;     if constexpr (!ALIGN_EPI) { if (wr == 0) PG8_BAR; }
;     PG8_BAR;
; template <int l>
; __device__ __forceinline__ void layer_body(const Args& args, unsigned char* lds, const XcdBarrier& bar, int G, int lo, int hi) {
;     ...
;                         __syncthreads(); }
;                     if (k < MOE_NGROUPS) { const int g = k, t0 = MOE_T0(g); int nM = nused - t0; nM = nM > MOE_GROUP ? MOE_GROUP : nM;
;                         S.init(args.ws + WS_XG, args.ws + WS_MUP, 1024, t0, nM, 28, G, (int)blockIdx.x); S.asub = 0; S.bes = (size_t)7168 * 1024 * 2;
;                         S.list = list1;
;                         pg8::EpiSwi E{(bf16*)(args.ws + WS_TM + (size_t)(g & 1) * 112 * MiB), DFFE, t0};
;                         pg8::gemm_phase<pg8::EpiSwi, pg8::SchedE>(L, 1024, S, E); }
.LBB0_2248:
	v_readlane_b32 s60, v254, 11
	v_readlane_b32 s20, v255, 46
	v_readlane_b32 s54, v255, 48
	v_readlane_b32 s56, v255, 50
	v_readlane_b32 s58, v255, 52
	v_readlane_b32 s62, v255, 54
	v_readlane_b32 s80, v255, 56
	v_readlane_b32 s92, v255, 58
	v_readlane_b32 s61, v254, 12
	v_readlane_b32 s21, v255, 47
	v_readlane_b32 s55, v255, 49
	v_readlane_b32 s57, v255, 51
	v_readlane_b32 s59, v255, 53
	v_readlane_b32 s63, v255, 55
	v_readlane_b32 s81, v255, 57
	v_readlane_b32 s93, v255, 59
	v_readlane_b32 s72, v255, 60
	v_readlane_b32 s73, v255, 62

; #define PG8_WAIT_V(n) asm volatile("s_waitcnt vmcnt(" #n ")" ::: "memory")
; #define PG8_BAR __builtin_amdgcn_s_barrier()
;     ...
;     PG8_WAIT_V(0);
;     if constexpr (!ALIGN_EPI) { if (wr == 0) PG8_BAR; }
;     PG8_BAR;
; template <int l>
; __device__ __forceinline__ void layer_body(const Args& args, unsigned char* lds, const XcdBarrier& bar, int G, int lo, int hi) {
;     ...
;                         __syncthreads(); }
;                     if (k < MOE_NGROUPS) { const int g = k, t0 = MOE_T0(g); int nM = nused - t0; nM = nM > MOE_GROUP ? MOE_GROUP : nM;
;                         S.init(args.ws + WS_XG, args.ws + WS_MUP, 1024, t0, nM, 28, G, (int)blockIdx.x); S.asub = 0; S.bes = (size_t)7168 * 1024 * 2;
;                         S.list = list1;
;                         pg8::EpiSwi E{(bf16*)(args.ws + WS_TM + (size_t)(g & 1) * 112 * MiB), DFFE, t0};
;                         pg8::gemm_phase<pg8::EpiSwi, pg8::SchedE>(L, 1024, S, E); }
.LBB0_4511:
	v_readlane_b32 s54, v254, 11
	v_readlane_b32 s56, v253, 6
	v_readlane_b32 s60, v254, 23
	v_readlane_b32 s62, v254, 32
	v_readlane_b32 s50, v253, 2
	v_readlane_b32 s78, v254, 8
	v_readlane_b32 s55, v254, 12
	v_readlane_b32 s57, v253, 7
	v_readlane_b32 s61, v254, 24
	v_readlane_b32 s63, v254, 33
	v_readlane_b32 s51, v253, 3
	v_readlane_b32 s65, v254, 38
	v_readlane_b32 s67, v255, 25
